# combo5 = combo4 + MoE plan tables built by a 64-lane prefix sum instead of a one-thread LDS walk
# speedup vs baseline: 1.1280x; 1.0515x over previous
.LBB0_151:
	v_or_b32_e32 v132, 16, v162
	v_ashrrev_i32_e32 v133, 31, v132
	v_lshl_add_u64 v[130:131], v[132:133], 2, s[16:17]
	v_mov_b32_e32 v130, v192
	v_cvt_f32_i32_e32 v127, v127
	v_cvt_f32_i32_e32 v126, v126
	v_cvt_f32_i32_e32 v129, v129
	v_cvt_f32_i32_e32 v128, v128
	v_cvt_f32_i32_e32 v137, v123
	v_cvt_f32_i32_e32 v136, v122
	v_cvt_f32_i32_e32 v139, v125
	v_cvt_f32_i32_e32 v138, v124
	v_mov_b64_e32 v[134:135], s[14:15]
	v_mad_i64_i32 v[122:123], s[30:31], v132, s64, v[134:135]
	v_pk_mul_f32 v[128:129], v[60:61], v[128:129]
	v_pk_mul_f32 v[126:127], v[58:59], v[126:127]
	v_pk_mul_f32 v[138:139], v[56:57], v[138:139]
	v_pk_mul_f32 v[136:137], v[54:55], v[136:137]
	s_and_b64 vcc, exec, s[6:7]
	v_lshl_add_u64 v[124:125], v[160:161], 1, v[122:123]
	s_mov_b64 s[30:31], -1
	s_nop 1
	v_pk_mul_f32 v[132:133], v[128:129], v[130:131] op_sel_hi:[1,0]
	v_pk_mul_f32 v[134:135], v[126:127], v[130:131] op_sel_hi:[1,0]
	v_pk_mul_f32 v[126:127], v[138:139], v[130:131] op_sel_hi:[1,0]
	v_pk_mul_f32 v[128:129], v[136:137], v[130:131] op_sel_hi:[1,0]
	s_cbranch_vccnz .LBB0_153
	s_mov_b64 s[30:31], 0
	v_cvt_pk_bf16_f32 v136, v134, v135
	v_cvt_pk_bf16_f32 v137, v132, v133
	v_cvt_pk_bf16_f32 v138, v128, v129
	v_cvt_pk_bf16_f32 v139, v126, v127
	global_store_dwordx4 v[124:125], v[136:139], off

.LBB0_159:
	v_or_b32_e32 v116, 32, v162
	v_ashrrev_i32_e32 v117, 31, v116
	v_lshl_add_u64 v[114:115], v[116:117], 2, s[16:17]
	v_mov_b32_e32 v114, v193
	v_cvt_f32_i32_e32 v111, v111
	v_cvt_f32_i32_e32 v110, v110
	v_cvt_f32_i32_e32 v113, v113
	v_cvt_f32_i32_e32 v112, v112
	v_cvt_f32_i32_e32 v121, v107
	v_cvt_f32_i32_e32 v120, v106
	v_cvt_f32_i32_e32 v123, v109
	v_cvt_f32_i32_e32 v122, v108
	v_mov_b64_e32 v[118:119], s[14:15]
	v_mad_i64_i32 v[106:107], s[30:31], v116, s64, v[118:119]
	v_pk_mul_f32 v[112:113], v[60:61], v[112:113]
	v_pk_mul_f32 v[110:111], v[58:59], v[110:111]
	v_pk_mul_f32 v[122:123], v[56:57], v[122:123]
	v_pk_mul_f32 v[120:121], v[54:55], v[120:121]
	s_and_b64 vcc, exec, s[6:7]
	v_lshl_add_u64 v[108:109], v[160:161], 1, v[106:107]
	s_mov_b64 s[30:31], -1
	s_nop 1
	v_pk_mul_f32 v[116:117], v[112:113], v[114:115] op_sel_hi:[1,0]
	v_pk_mul_f32 v[118:119], v[110:111], v[114:115] op_sel_hi:[1,0]
	v_pk_mul_f32 v[110:111], v[122:123], v[114:115] op_sel_hi:[1,0]
	v_pk_mul_f32 v[112:113], v[120:121], v[114:115] op_sel_hi:[1,0]
	s_cbranch_vccnz .LBB0_161
	s_mov_b64 s[30:31], 0
	v_cvt_pk_bf16_f32 v120, v118, v119
	v_cvt_pk_bf16_f32 v121, v116, v117
	v_cvt_pk_bf16_f32 v122, v112, v113
	v_cvt_pk_bf16_f32 v123, v110, v111
	global_store_dwordx4 v[108:109], v[120:123], off

.LBB0_167:
	v_or_b32_e32 v100, 48, v162
	v_ashrrev_i32_e32 v101, 31, v100
	v_lshl_add_u64 v[98:99], v[100:101], 2, s[16:17]
	v_mov_b32_e32 v98, v194
	v_cvt_f32_i32_e32 v95, v95
	v_cvt_f32_i32_e32 v94, v94
	v_cvt_f32_i32_e32 v97, v97
	v_cvt_f32_i32_e32 v96, v96
	v_cvt_f32_i32_e32 v105, v91
	v_cvt_f32_i32_e32 v104, v90
	v_cvt_f32_i32_e32 v107, v93
	v_cvt_f32_i32_e32 v106, v92
	v_mov_b64_e32 v[102:103], s[14:15]
	v_mad_i64_i32 v[90:91], s[30:31], v100, s64, v[102:103]
	v_pk_mul_f32 v[96:97], v[60:61], v[96:97]
	v_pk_mul_f32 v[94:95], v[58:59], v[94:95]
	v_pk_mul_f32 v[106:107], v[56:57], v[106:107]
	v_pk_mul_f32 v[104:105], v[54:55], v[104:105]
	s_and_b64 vcc, exec, s[6:7]
	v_lshl_add_u64 v[92:93], v[160:161], 1, v[90:91]
	s_mov_b64 s[30:31], -1
	s_nop 1
	v_pk_mul_f32 v[100:101], v[96:97], v[98:99] op_sel_hi:[1,0]
	v_pk_mul_f32 v[102:103], v[94:95], v[98:99] op_sel_hi:[1,0]
	v_pk_mul_f32 v[94:95], v[106:107], v[98:99] op_sel_hi:[1,0]
	v_pk_mul_f32 v[96:97], v[104:105], v[98:99] op_sel_hi:[1,0]
	s_cbranch_vccnz .LBB0_169
	s_mov_b64 s[30:31], 0
	v_cvt_pk_bf16_f32 v104, v102, v103
	v_cvt_pk_bf16_f32 v105, v100, v101
	v_cvt_pk_bf16_f32 v106, v96, v97
	v_cvt_pk_bf16_f32 v107, v94, v95
	global_store_dwordx4 v[92:93], v[104:107], off

.LBB0_175:
	v_mov_b32_e32 v82, v195
	v_cvt_f32_i32_e32 v79, v79
	v_cvt_f32_i32_e32 v78, v78
	v_cvt_f32_i32_e32 v81, v81
	v_cvt_f32_i32_e32 v80, v80
	v_cvt_f32_i32_e32 v87, v75
	v_cvt_f32_i32_e32 v86, v74
	v_cvt_f32_i32_e32 v89, v77
	v_cvt_f32_i32_e32 v88, v76
	v_add_u32_e32 v83, 0x80, v162
	v_mov_b64_e32 v[84:85], s[14:15]
	v_mad_i64_i32 v[74:75], s[30:31], v83, s64, v[84:85]
	v_pk_mul_f32 v[80:81], v[60:61], v[80:81]
	v_pk_mul_f32 v[78:79], v[58:59], v[78:79]
	v_pk_mul_f32 v[88:89], v[56:57], v[88:89]
	v_pk_mul_f32 v[90:91], v[54:55], v[86:87]
	s_and_b64 vcc, exec, s[6:7]
	v_lshl_add_u64 v[76:77], v[160:161], 1, v[74:75]
	s_mov_b64 s[30:31], -1
	s_nop 1
	v_pk_mul_f32 v[84:85], v[80:81], v[82:83] op_sel_hi:[1,0]
	v_pk_mul_f32 v[86:87], v[78:79], v[82:83] op_sel_hi:[1,0]
	v_pk_mul_f32 v[78:79], v[88:89], v[82:83] op_sel_hi:[1,0]
	v_pk_mul_f32 v[80:81], v[90:91], v[82:83] op_sel_hi:[1,0]
	s_cbranch_vccnz .LBB0_177
	s_mov_b64 s[30:31], 0
	v_cvt_pk_bf16_f32 v88, v86, v87
	v_cvt_pk_bf16_f32 v89, v84, v85
	v_cvt_pk_bf16_f32 v90, v80, v81
	v_cvt_pk_bf16_f32 v91, v78, v79
	global_store_dwordx4 v[76:77], v[88:91], off

.LBB0_183:
	v_mov_b32_e32 v66, v196
	v_cvt_f32_i32_e32 v63, v63
	v_cvt_f32_i32_e32 v62, v62
	v_cvt_f32_i32_e32 v65, v65
	v_cvt_f32_i32_e32 v64, v64
	v_cvt_f32_i32_e32 v71, v51
	v_cvt_f32_i32_e32 v70, v50
	v_cvt_f32_i32_e32 v73, v53
	v_cvt_f32_i32_e32 v72, v52
	v_add_u32_e32 v67, 0x90, v162
	v_mov_b64_e32 v[68:69], s[14:15]
	v_mad_i64_i32 v[50:51], s[30:31], v67, s64, v[68:69]
	v_pk_mul_f32 v[64:65], v[60:61], v[64:65]
	v_pk_mul_f32 v[62:63], v[58:59], v[62:63]
	v_pk_mul_f32 v[72:73], v[56:57], v[72:73]
	v_pk_mul_f32 v[74:75], v[54:55], v[70:71]
	s_and_b64 vcc, exec, s[6:7]
	v_lshl_add_u64 v[52:53], v[160:161], 1, v[50:51]
	s_mov_b64 s[30:31], -1
	s_nop 1
	v_pk_mul_f32 v[68:69], v[64:65], v[66:67] op_sel_hi:[1,0]
	v_pk_mul_f32 v[70:71], v[62:63], v[66:67] op_sel_hi:[1,0]
	v_pk_mul_f32 v[62:63], v[72:73], v[66:67] op_sel_hi:[1,0]
	v_pk_mul_f32 v[64:65], v[74:75], v[66:67] op_sel_hi:[1,0]
	s_cbranch_vccnz .LBB0_185
	s_mov_b64 s[30:31], 0
	v_cvt_pk_bf16_f32 v72, v70, v71
	v_cvt_pk_bf16_f32 v73, v68, v69
	v_cvt_pk_bf16_f32 v74, v64, v65
	v_cvt_pk_bf16_f32 v75, v62, v63
	global_store_dwordx4 v[52:53], v[72:75], off

.LBB0_191:
	v_mov_b32_e32 v34, v197
	v_cvt_f32_i32_e32 v31, v31
	v_cvt_f32_i32_e32 v30, v30
	v_cvt_f32_i32_e32 v33, v33
	v_cvt_f32_i32_e32 v32, v32
	v_cvt_f32_i32_e32 v39, v27
	v_cvt_f32_i32_e32 v38, v26
	v_cvt_f32_i32_e32 v41, v29
	v_cvt_f32_i32_e32 v40, v28
	v_add_u32_e32 v35, 0xa0, v162
	v_mov_b64_e32 v[36:37], s[14:15]
	v_mad_i64_i32 v[26:27], s[30:31], v35, s64, v[36:37]
	v_pk_mul_f32 v[32:33], v[60:61], v[32:33]
	v_pk_mul_f32 v[30:31], v[58:59], v[30:31]
	v_pk_mul_f32 v[40:41], v[56:57], v[40:41]
	v_pk_mul_f32 v[50:51], v[54:55], v[38:39]
	s_and_b64 vcc, exec, s[6:7]
	v_lshl_add_u64 v[28:29], v[160:161], 1, v[26:27]
	s_mov_b64 s[30:31], -1
	s_nop 1
	v_pk_mul_f32 v[36:37], v[32:33], v[34:35] op_sel_hi:[1,0]
	v_pk_mul_f32 v[38:39], v[30:31], v[34:35] op_sel_hi:[1,0]
	v_pk_mul_f32 v[30:31], v[40:41], v[34:35] op_sel_hi:[1,0]
	v_pk_mul_f32 v[32:33], v[50:51], v[34:35] op_sel_hi:[1,0]
	s_cbranch_vccnz .LBB0_193
	s_mov_b64 s[30:31], 0
	v_cvt_pk_bf16_f32 v50, v38, v39
	v_cvt_pk_bf16_f32 v51, v36, v37
	v_cvt_pk_bf16_f32 v52, v32, v33
	v_cvt_pk_bf16_f32 v53, v30, v31
	global_store_dwordx4 v[28:29], v[50:53], off

.LBB0_199:
	v_mov_b32_e32 v18, v198
	v_cvt_f32_i32_e32 v15, v15
	v_cvt_f32_i32_e32 v14, v14
	v_cvt_f32_i32_e32 v17, v17
	v_cvt_f32_i32_e32 v16, v16
	v_cvt_f32_i32_e32 v23, v11
	v_cvt_f32_i32_e32 v22, v10
	v_cvt_f32_i32_e32 v25, v13
	v_cvt_f32_i32_e32 v24, v12
	v_add_u32_e32 v19, 0xb0, v162
	v_mov_b64_e32 v[20:21], s[14:15]
	v_mad_i64_i32 v[10:11], s[30:31], v19, s64, v[20:21]
	v_pk_mul_f32 v[16:17], v[60:61], v[16:17]
	v_pk_mul_f32 v[14:15], v[58:59], v[14:15]
	v_pk_mul_f32 v[24:25], v[56:57], v[24:25]
	v_pk_mul_f32 v[26:27], v[54:55], v[22:23]
	s_and_b64 vcc, exec, s[6:7]
	v_lshl_add_u64 v[12:13], v[160:161], 1, v[10:11]
	s_mov_b64 s[30:31], -1
	s_nop 1
	v_pk_mul_f32 v[20:21], v[16:17], v[18:19] op_sel_hi:[1,0]
	v_pk_mul_f32 v[22:23], v[14:15], v[18:19] op_sel_hi:[1,0]
	v_pk_mul_f32 v[14:15], v[24:25], v[18:19] op_sel_hi:[1,0]
	v_pk_mul_f32 v[16:17], v[26:27], v[18:19] op_sel_hi:[1,0]
	s_cbranch_vccnz .LBB0_201
	s_mov_b64 s[30:31], 0
	v_cvt_pk_bf16_f32 v24, v22, v23
	v_cvt_pk_bf16_f32 v25, v20, v21
	v_cvt_pk_bf16_f32 v26, v16, v17
	v_cvt_pk_bf16_f32 v27, v14, v15
	global_store_dwordx4 v[12:13], v[24:27], off

.LBB0_1024:
	s_or_b64 exec, exec, s[4:5]
	s_waitcnt lgkmcnt(0)
	s_barrier
	v_cmp_gt_u32_e32 vcc, 64, v0
	s_and_saveexec_b64 s[4:5], vcc
	s_cbranch_execz .LBB0_1040
	v_mbcnt_lo_u32_b32 v2, -1, 0
	v_mbcnt_hi_u32_b32 v2, -1, v2
	v_add_u32_e32 v3, 0xff, v1
	v_lshrrev_b32_e32 v3, 8, v3
	v_mov_b32_e32 v4, v3
	v_subrev_u32_e32 v5, 1, v2
	v_lshlrev_b32_e32 v5, 2, v5
	ds_bpermute_b32 v6, v5, v4
	v_cmp_le_u32_e32 vcc, 1, v2
	s_waitcnt lgkmcnt(0)
	v_cndmask_b32_e32 v6, 0, v6, vcc
	v_add_u32_e32 v4, v4, v6
	v_subrev_u32_e32 v5, 2, v2
	v_lshlrev_b32_e32 v5, 2, v5
	ds_bpermute_b32 v6, v5, v4
	v_cmp_le_u32_e32 vcc, 2, v2
	s_waitcnt lgkmcnt(0)
	v_cndmask_b32_e32 v6, 0, v6, vcc
	v_add_u32_e32 v4, v4, v6
	v_subrev_u32_e32 v5, 4, v2
	v_lshlrev_b32_e32 v5, 2, v5
	ds_bpermute_b32 v6, v5, v4
	v_cmp_le_u32_e32 vcc, 4, v2
	s_waitcnt lgkmcnt(0)
	v_cndmask_b32_e32 v6, 0, v6, vcc
	v_add_u32_e32 v4, v4, v6
	v_subrev_u32_e32 v5, 8, v2
	v_lshlrev_b32_e32 v5, 2, v5
	ds_bpermute_b32 v6, v5, v4
	v_cmp_le_u32_e32 vcc, 8, v2
	s_waitcnt lgkmcnt(0)
	v_cndmask_b32_e32 v6, 0, v6, vcc
	v_add_u32_e32 v4, v4, v6
	v_subrev_u32_e32 v5, 16, v2
	v_lshlrev_b32_e32 v5, 2, v5
	ds_bpermute_b32 v6, v5, v4
	v_cmp_le_u32_e32 vcc, 16, v2
	s_waitcnt lgkmcnt(0)
	v_cndmask_b32_e32 v6, 0, v6, vcc
	v_add_u32_e32 v4, v4, v6
	v_subrev_u32_e32 v5, 32, v2
	v_lshlrev_b32_e32 v5, 2, v5
	ds_bpermute_b32 v6, v5, v4
	v_cmp_le_u32_e32 vcc, 32, v2
	s_waitcnt lgkmcnt(0)
	v_cndmask_b32_e32 v6, 0, v6, vcc
	v_add_u32_e32 v4, v4, v6
	s_movk_i32 s14, 0xc0
	v_sub_u32_e32 v5, v4, v3
	v_min_u32_e32 v5, s14, v5
	v_lshlrev_b32_e32 v7, 2, v2
	v_add_u32_e32 v7, 0x24000, v7
	ds_write_b32 v7, v5 offset:320
	v_readlane_b32 s6, v4, 63
	s_nop 3
	s_min_u32 s6, s6, s14
	v_mov_b32_e32 v8, s6
	v_mov_b32_e32 v9, 0x24240
	ds_write_b32 v9, v8
	v_mov_b32_e32 v9, 0x24580
	ds_write_b32 v9, v8
	v_mov_b32_e32 v6, 0
	v_lshlrev_b32_e32 v7, 2, v5
	v_add_u32_e32 v7, 0x24280, v7
.Lplan_fill:
	v_add_u32_e32 v9, v5, v6
	v_cmp_lt_u32_e32 vcc, v6, v3
	v_cmp_gt_u32_e64 s[8:9], s14, v9
	s_and_b64 s[8:9], vcc, s[8:9]
	s_and_b64 s[8:9], s[8:9], exec
	s_cbranch_scc0 .Lplan_done
	s_mov_b64 s[12:13], exec
	s_mov_b64 exec, s[8:9]
	ds_write_b32 v7, v2
	s_mov_b64 exec, s[12:13]
	v_add_u32_e32 v6, 1, v6
	v_add_u32_e32 v7, 4, v7
	s_branch .Lplan_fill
.Lplan_done:
.LBB0_1040:
	s_or_b64 exec, exec, s[4:5]
	s_add_i32 s4, 0, 0x24580
	v_mov_b32_e32 v1, s4
	s_waitcnt lgkmcnt(0)
	s_barrier
	ds_read_b32 v1, v1
	s_and_b32 s4, s2, 7
	s_ashr_i32 s5, s3, 3
	s_mul_i32 s44, s5, s4
	s_ashr_i32 s4, s2, 3
	s_waitcnt lgkmcnt(0)
	v_readfirstlane_b32 s45, v1
	s_andn2_b64 vcc, exec, s[10:11]
	s_add_i32 s44, s44, s4
	s_cbranch_vccnz .LBB0_1086
	s_load_dwordx2 s[6:7], s[0:1], 0xb0
	s_mul_i32 s25, s45, 6
	s_movk_i32 s4, 0x100
	v_cmp_gt_u32_e32 vcc, s4, v0
	s_mul_hi_i32 s19, s44, 0x2aaaaaab
	s_waitcnt lgkmcnt(0)
	s_add_u32 s12, s6, 0x3380a000
	s_addc_u32 s13, s7, 0
	s_add_i32 s18, 0, 0x24600
	s_cmp_lt_i32 s44, s25
	s_cselect_b64 s[8:9], -1, 0
	v_lshl_add_u32 v1, v0, 2, s18
	s_and_b64 s[4:5], s[8:9], vcc
	s_and_saveexec_b64 s[14:15], s[4:5]
	s_cbranch_execz .LBB0_1045
	s_lshr_b32 s4, s19, 31
	s_add_i32 s4, s19, s4
	s_lshl_b32 s5, s4, 2
	s_add_i32 s5, s5, 0
	s_add_i32 s5, s5, 0x24280
	s_waitcnt vmcnt(7)
	v_mov_b32_e32 v2, s5
	ds_read_b32 v2, v2
	s_waitcnt lgkmcnt(0)
	v_lshlrev_b32_e32 v3, 2, v2
	v_add_u32_e32 v3, 0, v3
	v_add_u32_e32 v4, 0x24140, v3
	ds_read_b32 v4, v4
	v_add_u32_e32 v3, 0x24040, v3
	ds_read_b32 v3, v3
	s_waitcnt lgkmcnt(1)
	v_sub_u32_e32 v4, s4, v4
	v_lshlrev_b32_e32 v4, 8, v4
	v_or_b32_e32 v5, v4, v0
	s_waitcnt lgkmcnt(0)
	v_cmp_lt_i32_e64 s[4:5], v5, v3
	v_mov_b32_e32 v3, 0
	s_and_saveexec_b64 s[16:17], s[4:5]
	s_cbranch_execz .LBB0_1044
	v_lshlrev_b32_e32 v2, 14, v2
	v_add_u32_e32 v2, v4, v2
	v_or_b32_e32 v2, v2, v0
	v_mov_b32_e32 v3, 0
	v_lshl_add_u64 v[2:3], v[2:3], 2, s[12:13]
	global_load_dword v3, v[2:3], off
